# hooks: second LDS read of each tile issued (unpredicated, spare quad) before the first predicated read/store block, so the two LDS read->store pairs no longer serialize
# baseline (speedup 1.0000x reference)
; #define GAS __attribute__((address_space(1)))
; #define LAS __attribute__((address_space(3)))
; #define LDS_BARRIER() do { asm volatile("s_waitcnt lgkmcnt(0)" ::: "memory"); __builtin_amdgcn_s_barrier(); asm volatile("" ::: "memory"); } while (0)
; __device__ __forceinline__ unsigned pk4_fp8(float a, float b, float c, float d) {
;     a = __builtin_amdgcn_fmed3f(a, -448.f, 448.f); b = __builtin_amdgcn_fmed3f(b, -448.f, 448.f); c = __builtin_amdgcn_fmed3f(c, -448.f, 448.f); d = __builtin_amdgcn_fmed3f(d, -448.f, 448.f);
;     int w = 0; w = __builtin_amdgcn_cvt_pk_fp8_f32(a, b, w, false); w = __builtin_amdgcn_cvt_pk_fp8_f32(c, d, w, true); return (unsigned)w; }
; template <class RowMap>
; __device__ __forceinline__ void conv_store_fp8(const f32x4 (&r)[8], unsigned char* WT, int Kbytes, int k0bytes, int n0, const RowMap rm, LAS unsigned char* T, int tid, int wave, int lane) {
;     const int s = 2 * (lane & 3);
; #pragma unroll
;     for (int j = 0; j < 4; ++j) { const unsigned lo = pk4_fp8(r[0][j] * W8_SCALE, r[1][j] * W8_SCALE, r[2][j] * W8_SCALE, r[3][j] * W8_SCALE), hi = pk4_fp8(r[4][j] * W8_SCALE, r[5][j] * W8_SCALE, r[6][j] * W8_SCALE, r[7][j] * W8_SCALE);
;         *(LAS unsigned long long*)(T + (4 * lane + j) * 64 + 8 * (wave ^ s)) = (unsigned long long)lo | ((unsigned long long)hi << 32); }
;     LDS_BARRIER();
;     const int c16 = tid & 3, rr = tid >> 2;
; #pragma unroll
;     for (int q = 0; q < 2; ++q) { const int row = rr + 128 * q; const v4u v = *(const LAS v4u*)(T + row * 64 + 16 * (c16 ^ ((row >> 2) & 3)));
;         const int dr = rm(n0 + row); if (dr >= 0) *(GAS v4u*)(WT + (unsigned)((((dr >> 8) * (Kbytes >> 7) + (k0bytes >> 7)) << 15) + ((dr & 255) << 7) + (k0bytes & 127) + 16 * c16)) = v; }
;     LDS_BARRIER();
; }
.Lhw_done_2:
	v_med3_f32 v131, v2, s101, v200
	v_med3_f32 v149, v6, s101, v200
	v_mov_b32_e32 v132, v130
	v_cvt_scalef32_pk_fp8_f32 v132, v131, v149, v201
	v_med3_f32 v133, v10, s101, v200
	v_med3_f32 v148, v14, s101, v200
	v_cvt_scalef32_pk_fp8_f32 v132, v133, v148, v201 op_sel:[0,0,0,1]
	v_med3_f32 v131, v18, s101, v200
	v_med3_f32 v165, v22, s101, v200
	v_mov_b32_e32 v133, v130
	v_cvt_scalef32_pk_fp8_f32 v133, v131, v165, v201
	v_med3_f32 v148, v30, s101, v200
	v_med3_f32 v149, v26, s101, v200
	v_cvt_scalef32_pk_fp8_f32 v133, v148, v149, v201 op_sel:[0,0,0,1]
	v_med3_f32 v131, v3, s101, v200
	v_med3_f32 v166, v7, s101, v200
	v_mov_b32_e32 v148, v130
	v_cvt_scalef32_pk_fp8_f32 v148, v131, v166, v201
	v_med3_f32 v149, v11, s101, v200
	v_med3_f32 v165, v15, s101, v200
	v_cvt_scalef32_pk_fp8_f32 v148, v149, v165, v201 op_sel:[0,0,0,1]
	v_med3_f32 v131, v19, s101, v200
	v_med3_f32 v167, v23, s101, v200
	v_mov_b32_e32 v149, v130
	v_cvt_scalef32_pk_fp8_f32 v149, v131, v167, v201
	v_med3_f32 v165, v31, s101, v200
	v_med3_f32 v166, v27, s101, v200
	v_cvt_scalef32_pk_fp8_f32 v149, v165, v166, v201 op_sel:[0,0,0,1]
	v_med3_f32 v131, v4, s101, v200
	s_cmp_lg_u32 s1, 0
	ds_write2_b64 v164, v[132:133], v[148:149] offset1:8
	v_med3_f32 v149, v8, s101, v200
	v_mov_b32_e32 v132, v130
	v_cvt_scalef32_pk_fp8_f32 v132, v131, v149, v201
	v_med3_f32 v133, v12, s101, v200
	v_med3_f32 v148, v16, s101, v200
	v_cvt_scalef32_pk_fp8_f32 v132, v133, v148, v201 op_sel:[0,0,0,1]
	v_med3_f32 v131, v20, s101, v200
	v_med3_f32 v165, v24, s101, v200
	v_mov_b32_e32 v133, v130
	v_cvt_scalef32_pk_fp8_f32 v133, v131, v165, v201
	v_med3_f32 v148, v32, s101, v200
	v_med3_f32 v149, v28, s101, v200
	v_cvt_scalef32_pk_fp8_f32 v133, v148, v149, v201 op_sel:[0,0,0,1]
	v_med3_f32 v131, v5, s101, v200
	v_med3_f32 v166, v9, s101, v200
	v_mov_b32_e32 v148, v130
	v_cvt_scalef32_pk_fp8_f32 v148, v131, v166, v201
	v_med3_f32 v149, v13, s101, v200
	v_med3_f32 v165, v17, s101, v200
	v_cvt_scalef32_pk_fp8_f32 v148, v149, v165, v201 op_sel:[0,0,0,1]
	v_med3_f32 v131, v21, s101, v200
	v_med3_f32 v167, v25, s101, v200
	v_mov_b32_e32 v149, v130
	v_cvt_scalef32_pk_fp8_f32 v149, v131, v167, v201
	v_med3_f32 v165, v33, s101, v200
	v_med3_f32 v166, v29, s101, v200
	v_cvt_scalef32_pk_fp8_f32 v149, v165, v166, v201 op_sel:[0,0,0,1]
	v_add_u32_e32 v131, s0, v156
	ds_write2_b64 v164, v[132:133], v[148:149] offset0:16 offset1:24
	s_cbranch_scc0 .LBB0_834
	s_lshl_b32 s6, s1, 7
	v_lshlrev_b32_e32 v148, 1, v131
	s_waitcnt lgkmcnt(0)
	s_barrier
	s_add_i32 s24, s6, 0xffffff00
	v_and_b32_e32 v133, 0x7f, v131
	v_and_b32_e32 v148, 0xffffff00, v148
	s_and_b32 s7, s64, 0x7f
	v_add_u32_e32 v148, s24, v148
	v_or_b32_e32 v133, s6, v133
	s_lshr_b32 s13, s64, 7
	v_add_u32_e32 v132, s7, v158
	v_cmp_lt_i32_e32 vcc, -1, v148
	v_lshlrev_b32_e32 v133, 7, v133
	v_add_u32_e32 v174, v157, v161
	ds_read_b128 v[170:173], v174
	s_and_saveexec_b64 s[6:7], vcc
	s_cbranch_execz .LBB0_831
	v_add_u32_e32 v149, v157, v159
	ds_read_b128 v[166:169], v149
	v_lshrrev_b32_e32 v148, 8, v148
	v_mul_u32_u24_e32 v148, s12, v148
	v_add_lshl_u32 v148, v148, s13, 15
	v_and_b32_e32 v149, 0x7f80, v133
	v_add3_u32 v148, v149, v132, v148
	s_waitcnt lgkmcnt(0)
	global_store_dwordx4 v148, v[166:169], s[40:41]
.LBB0_831:
	s_or_b64 exec, exec, s[6:7]
	v_add_lshl_u32 v148, s0, v160, 1
	v_and_b32_e32 v148, 0xffffff00, v148
	v_add_u32_e32 v148, s24, v148
	v_cmp_lt_i32_e32 vcc, -1, v148
	s_and_saveexec_b64 s[6:7], vcc
	s_cbranch_execz .LBB0_833
	v_add_u32_e32 v149, v157, v161
	v_lshrrev_b32_e32 v148, 8, v148
	v_mul_u32_u24_e32 v148, s12, v148
	v_add_lshl_u32 v148, v148, s13, 15
	v_and_b32_e32 v133, 0x7f80, v133
	v_add3_u32 v132, v133, v132, v148
	s_waitcnt lgkmcnt(0)
	global_store_dwordx4 v132, v[170:173], s[40:41]

; #define GAS __attribute__((address_space(1)))
; #define LAS __attribute__((address_space(3)))
; #define LDS_BARRIER() do { asm volatile("s_waitcnt lgkmcnt(0)" ::: "memory"); __builtin_amdgcn_s_barrier(); asm volatile("" ::: "memory"); } while (0)
; template <class RowMap>
; __device__ __forceinline__ void conv_store_fp8(const f32x4 (&r)[8], unsigned char* WT, int Kbytes, int k0bytes, int n0, const RowMap rm, LAS unsigned char* T, int tid, int wave, int lane) {
;     ...
;     const int c16 = tid & 3, rr = tid >> 2;
; #pragma unroll
;     for (int q = 0; q < 2; ++q) { const int row = rr + 128 * q; const v4u v = *(const LAS v4u*)(T + row * 64 + 16 * (c16 ^ ((row >> 2) & 3)));
;         const int dr = rm(n0 + row); if (dr >= 0) *(GAS v4u*)(WT + (unsigned)((((dr >> 8) * (Kbytes >> 7) + (k0bytes >> 7)) << 15) + ((dr & 255) << 7) + (k0bytes & 127) + 16 * c16)) = v; }
;     LDS_BARRIER();
.LBB0_834:
	s_and_b64 vcc, exec, s[6:7]
	s_cbranch_vccz .LBB0_840
	s_waitcnt lgkmcnt(0)
	s_barrier
	s_and_b32 s6, s64, 0x7f
	s_lshr_b32 s13, s64, 7
	v_add_u32_e32 v132, s6, v158
	v_cmp_lt_i32_e32 vcc, -1, v131
	v_add_u32_e32 v174, v157, v161
	ds_read_b128 v[170:173], v174
	s_and_saveexec_b64 s[6:7], vcc
	s_cbranch_execz .LBB0_837
	v_add_u32_e32 v133, v157, v159
	ds_read_b128 v[166:169], v133
	v_lshrrev_b32_e32 v133, 8, v131
	v_mul_u32_u24_e32 v133, s12, v133
	v_lshlrev_b32_e32 v131, 7, v131
	v_add_lshl_u32 v133, v133, s13, 15
	v_and_b32_e32 v131, 0x7f80, v131
	v_add3_u32 v131, v131, v132, v133
	s_waitcnt lgkmcnt(0)
	global_store_dwordx4 v131, v[166:169], s[40:41]
.LBB0_837:
	s_or_b64 exec, exec, s[6:7]
	v_add_u32_e32 v131, s0, v160
	v_cmp_lt_i32_e32 vcc, -1, v131
	s_and_saveexec_b64 s[6:7], vcc
	s_cbranch_execz .LBB0_839
	v_add_u32_e32 v133, v157, v161
	v_lshrrev_b32_e32 v133, 8, v131
	v_mul_u32_u24_e32 v133, s12, v133
	v_lshlrev_b32_e32 v131, 7, v131
	v_add_lshl_u32 v133, v133, s13, 15
	v_and_b32_e32 v131, 0x7f80, v131
	v_add3_u32 v131, v131, v132, v133
	s_waitcnt lgkmcnt(0)
	global_store_dwordx4 v131, v[170:173], s[40:41]

; #define GAS __attribute__((address_space(1)))
; #define LAS __attribute__((address_space(3)))
; #define LDS_BARRIER() do { asm volatile("s_waitcnt lgkmcnt(0)" ::: "memory"); __builtin_amdgcn_s_barrier(); asm volatile("" ::: "memory"); } while (0)
; __device__ __forceinline__ unsigned pk4_fp8(float a, float b, float c, float d) {
;     a = __builtin_amdgcn_fmed3f(a, -448.f, 448.f); b = __builtin_amdgcn_fmed3f(b, -448.f, 448.f); c = __builtin_amdgcn_fmed3f(c, -448.f, 448.f); d = __builtin_amdgcn_fmed3f(d, -448.f, 448.f);
;     int w = 0; w = __builtin_amdgcn_cvt_pk_fp8_f32(a, b, w, false); w = __builtin_amdgcn_cvt_pk_fp8_f32(c, d, w, true); return (unsigned)w; }
; template <class RowMap>
; __device__ __forceinline__ void conv_store_fp8(const f32x4 (&r)[8], unsigned char* WT, int Kbytes, int k0bytes, int n0, const RowMap rm, LAS unsigned char* T, int tid, int wave, int lane) {
;     const int s = 2 * (lane & 3);
; #pragma unroll
;     for (int j = 0; j < 4; ++j) { const unsigned lo = pk4_fp8(r[0][j] * W8_SCALE, r[1][j] * W8_SCALE, r[2][j] * W8_SCALE, r[3][j] * W8_SCALE), hi = pk4_fp8(r[4][j] * W8_SCALE, r[5][j] * W8_SCALE, r[6][j] * W8_SCALE, r[7][j] * W8_SCALE);
;         *(LAS unsigned long long*)(T + (4 * lane + j) * 64 + 8 * (wave ^ s)) = (unsigned long long)lo | ((unsigned long long)hi << 32); }
;     LDS_BARRIER();
;     const int c16 = tid & 3, rr = tid >> 2;
; #pragma unroll
;     for (int q = 0; q < 2; ++q) { const int row = rr + 128 * q; const v4u v = *(const LAS v4u*)(T + row * 64 + 16 * (c16 ^ ((row >> 2) & 3)));
;         const int dr = rm(n0 + row); if (dr >= 0) *(GAS v4u*)(WT + (unsigned)((((dr >> 8) * (Kbytes >> 7) + (k0bytes >> 7)) << 15) + ((dr & 255) << 7) + (k0bytes & 127) + 16 * c16)) = v; }
;     LDS_BARRIER();
; }
.Lhw_done_3:
	v_med3_f32 v131, v38, s101, v200
	v_med3_f32 v149, v42, s101, v200
	v_mov_b32_e32 v132, v130
	v_cvt_scalef32_pk_fp8_f32 v132, v131, v149, v201
	v_med3_f32 v133, v34, s101, v200
	v_med3_f32 v148, v46, s101, v200
	v_cvt_scalef32_pk_fp8_f32 v132, v133, v148, v201 op_sel:[0,0,0,1]
	v_med3_f32 v131, v50, s101, v200
	v_med3_f32 v165, v54, s101, v200
	v_mov_b32_e32 v133, v130
	v_cvt_scalef32_pk_fp8_f32 v133, v131, v165, v201
	v_med3_f32 v148, v62, s101, v200
	v_med3_f32 v149, v58, s101, v200
	v_cvt_scalef32_pk_fp8_f32 v133, v148, v149, v201 op_sel:[0,0,0,1]
	v_med3_f32 v131, v39, s101, v200
	v_med3_f32 v166, v43, s101, v200
	v_mov_b32_e32 v148, v130
	v_cvt_scalef32_pk_fp8_f32 v148, v131, v166, v201
	v_med3_f32 v149, v35, s101, v200
	v_med3_f32 v165, v47, s101, v200
	v_cvt_scalef32_pk_fp8_f32 v148, v149, v165, v201 op_sel:[0,0,0,1]
	v_med3_f32 v131, v51, s101, v200
	v_med3_f32 v167, v55, s101, v200
	v_mov_b32_e32 v149, v130
	v_cvt_scalef32_pk_fp8_f32 v149, v131, v167, v201
	v_med3_f32 v165, v63, s101, v200
	v_med3_f32 v166, v59, s101, v200
	v_cvt_scalef32_pk_fp8_f32 v149, v165, v166, v201 op_sel:[0,0,0,1]
	v_med3_f32 v131, v40, s101, v200
	s_cmp_lg_u32 s57, 0
	ds_write2_b64 v164, v[132:133], v[148:149] offset1:8
	v_med3_f32 v149, v44, s101, v200
	v_mov_b32_e32 v132, v130
	v_cvt_scalef32_pk_fp8_f32 v132, v131, v149, v201
	v_med3_f32 v133, v36, s101, v200
	v_med3_f32 v148, v48, s101, v200
	v_cvt_scalef32_pk_fp8_f32 v132, v133, v148, v201 op_sel:[0,0,0,1]
	v_med3_f32 v131, v52, s101, v200
	v_med3_f32 v165, v56, s101, v200
	v_mov_b32_e32 v133, v130
	v_cvt_scalef32_pk_fp8_f32 v133, v131, v165, v201
	v_med3_f32 v148, v64, s101, v200
	v_med3_f32 v149, v60, s101, v200
	v_cvt_scalef32_pk_fp8_f32 v133, v148, v149, v201 op_sel:[0,0,0,1]
	v_med3_f32 v131, v41, s101, v200
	v_med3_f32 v166, v45, s101, v200
	v_mov_b32_e32 v148, v130
	v_cvt_scalef32_pk_fp8_f32 v148, v131, v166, v201
	v_med3_f32 v149, v37, s101, v200
	v_med3_f32 v165, v49, s101, v200
	v_cvt_scalef32_pk_fp8_f32 v148, v149, v165, v201 op_sel:[0,0,0,1]
	v_med3_f32 v131, v53, s101, v200
	v_med3_f32 v167, v57, s101, v200
	v_mov_b32_e32 v149, v130
	v_cvt_scalef32_pk_fp8_f32 v149, v131, v167, v201
	v_med3_f32 v165, v65, s101, v200
	v_med3_f32 v166, v61, s101, v200
	v_cvt_scalef32_pk_fp8_f32 v149, v165, v166, v201 op_sel:[0,0,0,1]
	v_add_u32_e32 v131, s56, v156
	ds_write2_b64 v164, v[132:133], v[148:149] offset0:16 offset1:24
	s_cbranch_scc0 .LBB0_870
	s_lshl_b32 s6, s57, 7
	v_lshlrev_b32_e32 v148, 1, v131
	s_waitcnt lgkmcnt(0)
	s_barrier
	s_add_i32 s24, s6, 0xffffff00
	v_and_b32_e32 v133, 0x7f, v131
	v_and_b32_e32 v148, 0xffffff00, v148
	s_and_b32 s7, s58, 0x7f
	v_add_u32_e32 v148, s24, v148
	v_or_b32_e32 v133, s6, v133
	s_lshr_b32 s13, s58, 7
	v_add_u32_e32 v132, s7, v158
	v_cmp_lt_i32_e32 vcc, -1, v148
	v_lshlrev_b32_e32 v133, 7, v133
	v_add_u32_e32 v174, v157, v161
	ds_read_b128 v[170:173], v174
	s_and_saveexec_b64 s[6:7], vcc
	s_cbranch_execz .LBB0_867
	v_add_u32_e32 v149, v157, v159
	ds_read_b128 v[166:169], v149
	v_lshrrev_b32_e32 v148, 8, v148
	v_mul_u32_u24_e32 v148, s12, v148
	v_add_lshl_u32 v148, v148, s13, 15
	v_and_b32_e32 v149, 0x7f80, v133
	v_add3_u32 v148, v149, v132, v148
	s_waitcnt lgkmcnt(0)
	global_store_dwordx4 v148, v[166:169], s[86:87]
.LBB0_867:
	s_or_b64 exec, exec, s[6:7]
	v_add_lshl_u32 v148, s56, v160, 1
	v_and_b32_e32 v148, 0xffffff00, v148
	v_add_u32_e32 v148, s24, v148
	v_cmp_lt_i32_e32 vcc, -1, v148
	s_and_saveexec_b64 s[6:7], vcc
	s_cbranch_execz .LBB0_869
	v_add_u32_e32 v149, v157, v161
	v_lshrrev_b32_e32 v148, 8, v148
	v_mul_u32_u24_e32 v148, s12, v148
	v_add_lshl_u32 v148, v148, s13, 15
	v_and_b32_e32 v133, 0x7f80, v133
	v_add3_u32 v132, v133, v132, v148
	s_waitcnt lgkmcnt(0)
	global_store_dwordx4 v132, v[170:173], s[86:87]

; #define GAS __attribute__((address_space(1)))
; #define LAS __attribute__((address_space(3)))
; #define LDS_BARRIER() do { asm volatile("s_waitcnt lgkmcnt(0)" ::: "memory"); __builtin_amdgcn_s_barrier(); asm volatile("" ::: "memory"); } while (0)
; template <class RowMap>
; __device__ __forceinline__ void conv_store_fp8(const f32x4 (&r)[8], unsigned char* WT, int Kbytes, int k0bytes, int n0, const RowMap rm, LAS unsigned char* T, int tid, int wave, int lane) {
;     ...
;     const int c16 = tid & 3, rr = tid >> 2;
; #pragma unroll
;     for (int q = 0; q < 2; ++q) { const int row = rr + 128 * q; const v4u v = *(const LAS v4u*)(T + row * 64 + 16 * (c16 ^ ((row >> 2) & 3)));
;         const int dr = rm(n0 + row); if (dr >= 0) *(GAS v4u*)(WT + (unsigned)((((dr >> 8) * (Kbytes >> 7) + (k0bytes >> 7)) << 15) + ((dr & 255) << 7) + (k0bytes & 127) + 16 * c16)) = v; }
;     LDS_BARRIER();
.LBB0_870:
	s_and_b64 vcc, exec, s[6:7]
	s_cbranch_vccz .LBB0_876
	s_waitcnt lgkmcnt(0)
	s_barrier
	s_and_b32 s6, s58, 0x7f
	s_lshr_b32 s13, s58, 7
	v_add_u32_e32 v132, s6, v158
	v_cmp_lt_i32_e32 vcc, -1, v131
	v_add_u32_e32 v174, v157, v161
	ds_read_b128 v[170:173], v174
	s_and_saveexec_b64 s[6:7], vcc
	s_cbranch_execz .LBB0_873
	v_add_u32_e32 v133, v157, v159
	ds_read_b128 v[166:169], v133
	v_lshrrev_b32_e32 v133, 8, v131
	v_mul_u32_u24_e32 v133, s12, v133
	v_lshlrev_b32_e32 v131, 7, v131
	v_add_lshl_u32 v133, v133, s13, 15
	v_and_b32_e32 v131, 0x7f80, v131
	v_add3_u32 v131, v131, v132, v133
	s_waitcnt lgkmcnt(0)
	global_store_dwordx4 v131, v[166:169], s[86:87]
.LBB0_873:
	s_or_b64 exec, exec, s[6:7]
	v_add_u32_e32 v131, s56, v160
	v_cmp_lt_i32_e32 vcc, -1, v131
	s_and_saveexec_b64 s[6:7], vcc
	s_cbranch_execz .LBB0_875
	v_add_u32_e32 v133, v157, v161
	v_lshrrev_b32_e32 v133, 8, v131
	v_mul_u32_u24_e32 v133, s12, v133
	v_lshlrev_b32_e32 v131, 7, v131
	v_add_lshl_u32 v133, v133, s13, 15
	v_and_b32_e32 v131, 0x7f80, v131
	v_add3_u32 v131, v131, v132, v133
	s_waitcnt lgkmcnt(0)
	global_store_dwordx4 v131, v[170:173], s[86:87]

; #define GAS __attribute__((address_space(1)))
; #define LAS __attribute__((address_space(3)))
; #define LDS_BARRIER() do { asm volatile("s_waitcnt lgkmcnt(0)" ::: "memory"); __builtin_amdgcn_s_barrier(); asm volatile("" ::: "memory"); } while (0)
; __device__ __forceinline__ unsigned pk4_fp8(float a, float b, float c, float d) {
;     a = __builtin_amdgcn_fmed3f(a, -448.f, 448.f); b = __builtin_amdgcn_fmed3f(b, -448.f, 448.f); c = __builtin_amdgcn_fmed3f(c, -448.f, 448.f); d = __builtin_amdgcn_fmed3f(d, -448.f, 448.f);
;     int w = 0; w = __builtin_amdgcn_cvt_pk_fp8_f32(a, b, w, false); w = __builtin_amdgcn_cvt_pk_fp8_f32(c, d, w, true); return (unsigned)w; }
; template <class RowMap>
; __device__ __forceinline__ void conv_store_fp8(const f32x4 (&r)[8], unsigned char* WT, int Kbytes, int k0bytes, int n0, const RowMap rm, LAS unsigned char* T, int tid, int wave, int lane) {
;     const int s = 2 * (lane & 3);
; #pragma unroll
;     for (int j = 0; j < 4; ++j) { const unsigned lo = pk4_fp8(r[0][j] * W8_SCALE, r[1][j] * W8_SCALE, r[2][j] * W8_SCALE, r[3][j] * W8_SCALE), hi = pk4_fp8(r[4][j] * W8_SCALE, r[5][j] * W8_SCALE, r[6][j] * W8_SCALE, r[7][j] * W8_SCALE);
;         *(LAS unsigned long long*)(T + (4 * lane + j) * 64 + 8 * (wave ^ s)) = (unsigned long long)lo | ((unsigned long long)hi << 32); }
;     LDS_BARRIER();
;     const int c16 = tid & 3, rr = tid >> 2;
; #pragma unroll
;     for (int q = 0; q < 2; ++q) { const int row = rr + 128 * q; const v4u v = *(const LAS v4u*)(T + row * 64 + 16 * (c16 ^ ((row >> 2) & 3)));
;         const int dr = rm(n0 + row); if (dr >= 0) *(GAS v4u*)(WT + (unsigned)((((dr >> 8) * (Kbytes >> 7) + (k0bytes >> 7)) << 15) + ((dr & 255) << 7) + (k0bytes & 127) + 16 * c16)) = v; }
;     LDS_BARRIER();
; }
.Lhw_done_4:
	v_med3_f32 v131, v70, s101, v200
	v_med3_f32 v149, v74, s101, v200
	v_mov_b32_e32 v132, v130
	v_cvt_scalef32_pk_fp8_f32 v132, v131, v149, v201
	v_med3_f32 v133, v66, s101, v200
	v_med3_f32 v148, v78, s101, v200
	v_cvt_scalef32_pk_fp8_f32 v132, v133, v148, v201 op_sel:[0,0,0,1]
	v_med3_f32 v131, v82, s101, v200
	v_med3_f32 v165, v86, s101, v200
	v_mov_b32_e32 v133, v130
	v_cvt_scalef32_pk_fp8_f32 v133, v131, v165, v201
	v_med3_f32 v148, v94, s101, v200
	v_med3_f32 v149, v90, s101, v200
	v_cvt_scalef32_pk_fp8_f32 v133, v148, v149, v201 op_sel:[0,0,0,1]
	v_med3_f32 v131, v71, s101, v200
	v_med3_f32 v166, v75, s101, v200
	v_mov_b32_e32 v148, v130
	v_cvt_scalef32_pk_fp8_f32 v148, v131, v166, v201
	v_med3_f32 v149, v67, s101, v200
	v_med3_f32 v165, v79, s101, v200
	v_cvt_scalef32_pk_fp8_f32 v148, v149, v165, v201 op_sel:[0,0,0,1]
	v_med3_f32 v131, v83, s101, v200
	v_med3_f32 v167, v87, s101, v200
	v_mov_b32_e32 v149, v130
	v_cvt_scalef32_pk_fp8_f32 v149, v131, v167, v201
	v_med3_f32 v165, v95, s101, v200
	v_med3_f32 v166, v91, s101, v200
	v_cvt_scalef32_pk_fp8_f32 v149, v165, v166, v201 op_sel:[0,0,0,1]
	v_med3_f32 v131, v72, s101, v200
	s_cmp_lg_u32 s27, 0
	ds_write2_b64 v164, v[132:133], v[148:149] offset1:8
	v_med3_f32 v149, v76, s101, v200
	v_mov_b32_e32 v132, v130
	v_cvt_scalef32_pk_fp8_f32 v132, v131, v149, v201
	v_med3_f32 v133, v68, s101, v200
	v_med3_f32 v148, v80, s101, v200
	v_cvt_scalef32_pk_fp8_f32 v132, v133, v148, v201 op_sel:[0,0,0,1]
	v_med3_f32 v131, v84, s101, v200
	v_med3_f32 v165, v88, s101, v200
	v_mov_b32_e32 v133, v130
	v_cvt_scalef32_pk_fp8_f32 v133, v131, v165, v201
	v_med3_f32 v148, v96, s101, v200
	v_med3_f32 v149, v92, s101, v200
	v_cvt_scalef32_pk_fp8_f32 v133, v148, v149, v201 op_sel:[0,0,0,1]
	v_med3_f32 v131, v73, s101, v200
	v_med3_f32 v166, v77, s101, v200
	v_mov_b32_e32 v148, v130
	v_cvt_scalef32_pk_fp8_f32 v148, v131, v166, v201
	v_med3_f32 v149, v69, s101, v200
	v_med3_f32 v165, v81, s101, v200
	v_cvt_scalef32_pk_fp8_f32 v148, v149, v165, v201 op_sel:[0,0,0,1]
	v_med3_f32 v131, v85, s101, v200
	v_med3_f32 v167, v89, s101, v200
	v_mov_b32_e32 v149, v130
	v_cvt_scalef32_pk_fp8_f32 v149, v131, v167, v201
	v_med3_f32 v165, v97, s101, v200
	v_med3_f32 v166, v93, s101, v200
	v_cvt_scalef32_pk_fp8_f32 v149, v165, v166, v201 op_sel:[0,0,0,1]
	v_add_u32_e32 v131, s20, v156
	ds_write2_b64 v164, v[132:133], v[148:149] offset0:16 offset1:24
	s_cbranch_scc0 .LBB0_905
	s_lshl_b32 s6, s27, 7
	v_lshlrev_b32_e32 v148, 1, v131
	s_waitcnt lgkmcnt(0)
	s_barrier
	s_add_i32 s24, s6, 0xffffff00
	v_and_b32_e32 v133, 0x7f, v131
	v_and_b32_e32 v148, 0xffffff00, v148
	s_and_b32 s7, s29, 0x7f
	v_add_u32_e32 v148, s24, v148
	v_or_b32_e32 v133, s6, v133
	s_lshr_b32 s13, s29, 7
	v_add_u32_e32 v132, s7, v158
	v_cmp_lt_i32_e32 vcc, -1, v148
	v_lshlrev_b32_e32 v133, 7, v133
	v_add_u32_e32 v174, v157, v161
	ds_read_b128 v[170:173], v174
	s_and_saveexec_b64 s[6:7], vcc
	s_cbranch_execz .LBB0_902
	v_add_u32_e32 v149, v157, v159
	ds_read_b128 v[166:169], v149
	v_lshrrev_b32_e32 v148, 8, v148
	v_mul_u32_u24_e32 v148, s12, v148
	v_add_lshl_u32 v148, v148, s13, 15
	v_and_b32_e32 v149, 0x7f80, v133
	v_add3_u32 v148, v149, v132, v148
	s_waitcnt lgkmcnt(0)
	global_store_dwordx4 v148, v[166:169], s[90:91]
.LBB0_902:
	s_or_b64 exec, exec, s[6:7]
	v_add_lshl_u32 v148, s20, v160, 1
	v_and_b32_e32 v148, 0xffffff00, v148
	v_add_u32_e32 v148, s24, v148
	v_cmp_lt_i32_e32 vcc, -1, v148
	s_and_saveexec_b64 s[6:7], vcc
	s_cbranch_execz .LBB0_904
	v_add_u32_e32 v149, v157, v161
	v_lshrrev_b32_e32 v148, 8, v148
	v_mul_u32_u24_e32 v148, s12, v148
	v_add_lshl_u32 v148, v148, s13, 15
	v_and_b32_e32 v133, 0x7f80, v133
	v_add3_u32 v132, v133, v132, v148
	s_waitcnt lgkmcnt(0)
	global_store_dwordx4 v132, v[170:173], s[90:91]

; #define GAS __attribute__((address_space(1)))
; #define LAS __attribute__((address_space(3)))
; #define LDS_BARRIER() do { asm volatile("s_waitcnt lgkmcnt(0)" ::: "memory"); __builtin_amdgcn_s_barrier(); asm volatile("" ::: "memory"); } while (0)
; template <class RowMap>
; __device__ __forceinline__ void conv_store_fp8(const f32x4 (&r)[8], unsigned char* WT, int Kbytes, int k0bytes, int n0, const RowMap rm, LAS unsigned char* T, int tid, int wave, int lane) {
;     ...
;     const int c16 = tid & 3, rr = tid >> 2;
; #pragma unroll
;     for (int q = 0; q < 2; ++q) { const int row = rr + 128 * q; const v4u v = *(const LAS v4u*)(T + row * 64 + 16 * (c16 ^ ((row >> 2) & 3)));
;         const int dr = rm(n0 + row); if (dr >= 0) *(GAS v4u*)(WT + (unsigned)((((dr >> 8) * (Kbytes >> 7) + (k0bytes >> 7)) << 15) + ((dr & 255) << 7) + (k0bytes & 127) + 16 * c16)) = v; }
;     LDS_BARRIER();
.LBB0_905:
	s_and_b64 vcc, exec, s[6:7]
	s_cbranch_vccz .LBB0_911
	s_waitcnt lgkmcnt(0)
	s_barrier
	s_and_b32 s6, s29, 0x7f
	s_lshr_b32 s13, s29, 7
	v_add_u32_e32 v132, s6, v158
	v_cmp_lt_i32_e32 vcc, -1, v131
	v_add_u32_e32 v174, v157, v161
	ds_read_b128 v[170:173], v174
	s_and_saveexec_b64 s[6:7], vcc
	s_cbranch_execz .LBB0_908
	v_add_u32_e32 v133, v157, v159
	ds_read_b128 v[166:169], v133
	v_lshrrev_b32_e32 v133, 8, v131
	v_mul_u32_u24_e32 v133, s12, v133
	v_lshlrev_b32_e32 v131, 7, v131
	v_add_lshl_u32 v133, v133, s13, 15
	v_and_b32_e32 v131, 0x7f80, v131
	v_add3_u32 v131, v131, v132, v133
	s_waitcnt lgkmcnt(0)
	global_store_dwordx4 v131, v[166:169], s[90:91]
.LBB0_908:
	s_or_b64 exec, exec, s[6:7]
	v_add_u32_e32 v131, s20, v160
	v_cmp_lt_i32_e32 vcc, -1, v131
	s_and_saveexec_b64 s[6:7], vcc
	s_cbranch_execz .LBB0_910
	v_add_u32_e32 v133, v157, v161
	v_lshrrev_b32_e32 v133, 8, v131
	v_mul_u32_u24_e32 v133, s12, v133
	v_lshlrev_b32_e32 v131, 7, v131
	v_add_lshl_u32 v133, v133, s13, 15
	v_and_b32_e32 v131, 0x7f80, v131
	v_add3_u32 v131, v131, v132, v133
	s_waitcnt lgkmcnt(0)
	global_store_dwordx4 v131, v[170:173], s[90:91]

; #define GAS __attribute__((address_space(1)))
; #define LAS __attribute__((address_space(3)))
; #define LDS_BARRIER() do { asm volatile("s_waitcnt lgkmcnt(0)" ::: "memory"); __builtin_amdgcn_s_barrier(); asm volatile("" ::: "memory"); } while (0)
; __device__ __forceinline__ unsigned pk4_fp8(float a, float b, float c, float d) {
;     a = __builtin_amdgcn_fmed3f(a, -448.f, 448.f); b = __builtin_amdgcn_fmed3f(b, -448.f, 448.f); c = __builtin_amdgcn_fmed3f(c, -448.f, 448.f); d = __builtin_amdgcn_fmed3f(d, -448.f, 448.f);
;     int w = 0; w = __builtin_amdgcn_cvt_pk_fp8_f32(a, b, w, false); w = __builtin_amdgcn_cvt_pk_fp8_f32(c, d, w, true); return (unsigned)w; }
; template <class RowMap>
; __device__ __forceinline__ void conv_store_fp8(const f32x4 (&r)[8], unsigned char* WT, int Kbytes, int k0bytes, int n0, const RowMap rm, LAS unsigned char* T, int tid, int wave, int lane) {
;     const int s = 2 * (lane & 3);
; #pragma unroll
;     for (int j = 0; j < 4; ++j) { const unsigned lo = pk4_fp8(r[0][j] * W8_SCALE, r[1][j] * W8_SCALE, r[2][j] * W8_SCALE, r[3][j] * W8_SCALE), hi = pk4_fp8(r[4][j] * W8_SCALE, r[5][j] * W8_SCALE, r[6][j] * W8_SCALE, r[7][j] * W8_SCALE);
;         *(LAS unsigned long long*)(T + (4 * lane + j) * 64 + 8 * (wave ^ s)) = (unsigned long long)lo | ((unsigned long long)hi << 32); }
;     LDS_BARRIER();
;     const int c16 = tid & 3, rr = tid >> 2;
; #pragma unroll
;     for (int q = 0; q < 2; ++q) { const int row = rr + 128 * q; const v4u v = *(const LAS v4u*)(T + row * 64 + 16 * (c16 ^ ((row >> 2) & 3)));
;         const int dr = rm(n0 + row); if (dr >= 0) *(GAS v4u*)(WT + (unsigned)((((dr >> 8) * (Kbytes >> 7) + (k0bytes >> 7)) << 15) + ((dr & 255) << 7) + (k0bytes & 127) + 16 * c16)) = v; }
;     LDS_BARRIER();
; }
.Lhw_done_5:
	v_med3_f32 v131, v102, s101, v200
	v_med3_f32 v149, v106, s101, v200
	v_mov_b32_e32 v132, v130
	v_cvt_scalef32_pk_fp8_f32 v132, v131, v149, v201
	v_med3_f32 v133, v98, s101, v200
	v_med3_f32 v148, v110, s101, v200
	v_cvt_scalef32_pk_fp8_f32 v132, v133, v148, v201 op_sel:[0,0,0,1]
	v_med3_f32 v131, v114, s101, v200
	v_med3_f32 v165, v118, s101, v200
	v_mov_b32_e32 v133, v130
	v_cvt_scalef32_pk_fp8_f32 v133, v131, v165, v201
	v_med3_f32 v148, v126, s101, v200
	v_med3_f32 v149, v122, s101, v200
	v_cvt_scalef32_pk_fp8_f32 v133, v148, v149, v201 op_sel:[0,0,0,1]
	v_med3_f32 v131, v103, s101, v200
	v_med3_f32 v166, v107, s101, v200
	v_mov_b32_e32 v148, v130
	v_cvt_scalef32_pk_fp8_f32 v148, v131, v166, v201
	v_med3_f32 v149, v99, s101, v200
	v_med3_f32 v165, v111, s101, v200
	v_cvt_scalef32_pk_fp8_f32 v148, v149, v165, v201 op_sel:[0,0,0,1]
	v_med3_f32 v131, v115, s101, v200
	v_med3_f32 v167, v119, s101, v200
	v_mov_b32_e32 v149, v130
	v_cvt_scalef32_pk_fp8_f32 v149, v131, v167, v201
	v_med3_f32 v165, v127, s101, v200
	v_med3_f32 v166, v123, s101, v200
	v_cvt_scalef32_pk_fp8_f32 v149, v165, v166, v201 op_sel:[0,0,0,1]
	v_med3_f32 v131, v104, s101, v200
	s_cmp_lg_u32 s24, 0
	ds_write2_b64 v164, v[132:133], v[148:149] offset1:8
	v_med3_f32 v149, v108, s101, v200
	v_mov_b32_e32 v132, v130
	v_cvt_scalef32_pk_fp8_f32 v132, v131, v149, v201
	v_med3_f32 v133, v100, s101, v200
	v_med3_f32 v148, v112, s101, v200
	v_cvt_scalef32_pk_fp8_f32 v132, v133, v148, v201 op_sel:[0,0,0,1]
	v_med3_f32 v131, v116, s101, v200
	v_med3_f32 v165, v120, s101, v200
	v_mov_b32_e32 v133, v130
	v_cvt_scalef32_pk_fp8_f32 v133, v131, v165, v201
	v_med3_f32 v148, v128, s101, v200
	v_med3_f32 v149, v124, s101, v200
	v_cvt_scalef32_pk_fp8_f32 v133, v148, v149, v201 op_sel:[0,0,0,1]
	v_med3_f32 v131, v105, s101, v200
	v_med3_f32 v166, v109, s101, v200
	v_mov_b32_e32 v148, v130
	v_cvt_scalef32_pk_fp8_f32 v148, v131, v166, v201
	v_med3_f32 v149, v101, s101, v200
	v_med3_f32 v165, v113, s101, v200
	v_cvt_scalef32_pk_fp8_f32 v148, v149, v165, v201 op_sel:[0,0,0,1]
	v_med3_f32 v131, v117, s101, v200
	v_med3_f32 v167, v121, s101, v200
	v_mov_b32_e32 v149, v130
	v_cvt_scalef32_pk_fp8_f32 v149, v131, v167, v201
	v_med3_f32 v165, v129, s101, v200
	v_med3_f32 v166, v125, s101, v200
	v_cvt_scalef32_pk_fp8_f32 v149, v165, v166, v201 op_sel:[0,0,0,1]
	v_add_u32_e32 v131, s19, v156
	ds_write2_b64 v164, v[132:133], v[148:149] offset0:16 offset1:24
	s_cbranch_scc0 .LBB0_941
	s_waitcnt lgkmcnt(0)
	s_lshl_b32 s4, s24, 7
	v_lshlrev_b32_e32 v148, 1, v131
	s_waitcnt lgkmcnt(0)
	s_barrier
	s_add_i32 s7, s4, 0xffffff00
	v_and_b32_e32 v133, 0x7f, v131
	v_and_b32_e32 v148, 0xffffff00, v148
	s_and_b32 s5, s18, 0x7f
	v_add_u32_e32 v148, s7, v148
	v_or_b32_e32 v133, s4, v133
	s_lshr_b32 s6, s18, 7
	v_add_u32_e32 v132, s5, v158
	v_cmp_lt_i32_e32 vcc, -1, v148
	v_lshlrev_b32_e32 v133, 7, v133
	v_add_u32_e32 v174, v157, v161
	ds_read_b128 v[170:173], v174
	s_and_saveexec_b64 s[4:5], vcc
	s_cbranch_execz .LBB0_938
	v_add_u32_e32 v149, v157, v159
	ds_read_b128 v[166:169], v149
	v_lshrrev_b32_e32 v148, 8, v148
	v_mul_u32_u24_e32 v148, s2, v148
	v_add_lshl_u32 v148, v148, s6, 15
	v_and_b32_e32 v149, 0x7f80, v133
	v_add3_u32 v148, v149, v132, v148
	s_waitcnt lgkmcnt(0)
	global_store_dwordx4 v148, v[166:169], s[50:51]
.LBB0_938:
	s_or_b64 exec, exec, s[4:5]
	v_add_lshl_u32 v148, s19, v160, 1
	v_and_b32_e32 v148, 0xffffff00, v148
	v_add_u32_e32 v148, s7, v148
	v_cmp_lt_i32_e32 vcc, -1, v148
	s_and_saveexec_b64 s[4:5], vcc
	s_cbranch_execz .LBB0_940
	v_add_u32_e32 v149, v157, v161
	v_lshrrev_b32_e32 v148, 8, v148
	v_mul_u32_u24_e32 v148, s2, v148
	v_add_lshl_u32 v148, v148, s6, 15
	v_and_b32_e32 v133, 0x7f80, v133
	v_add3_u32 v132, v133, v132, v148
	s_waitcnt lgkmcnt(0)
	global_store_dwordx4 v132, v[170:173], s[50:51]

; #define GAS __attribute__((address_space(1)))
; #define LAS __attribute__((address_space(3)))
; #define LDS_BARRIER() do { asm volatile("s_waitcnt lgkmcnt(0)" ::: "memory"); __builtin_amdgcn_s_barrier(); asm volatile("" ::: "memory"); } while (0)
; template <class RowMap>
; __device__ __forceinline__ void conv_store_fp8(const f32x4 (&r)[8], unsigned char* WT, int Kbytes, int k0bytes, int n0, const RowMap rm, LAS unsigned char* T, int tid, int wave, int lane) {
;     ...
;     const int c16 = tid & 3, rr = tid >> 2;
; #pragma unroll
;     for (int q = 0; q < 2; ++q) { const int row = rr + 128 * q; const v4u v = *(const LAS v4u*)(T + row * 64 + 16 * (c16 ^ ((row >> 2) & 3)));
;         const int dr = rm(n0 + row); if (dr >= 0) *(GAS v4u*)(WT + (unsigned)((((dr >> 8) * (Kbytes >> 7) + (k0bytes >> 7)) << 15) + ((dr & 255) << 7) + (k0bytes & 127) + 16 * c16)) = v; }
;     LDS_BARRIER();
.LBB0_941:
	s_waitcnt lgkmcnt(0)
	s_cbranch_execz .LBB0_802
	s_waitcnt lgkmcnt(0)
	s_barrier
	s_and_b32 s4, s18, 0x7f
	s_lshr_b32 s6, s18, 7
	v_add_u32_e32 v132, s4, v158
	v_cmp_lt_i32_e32 vcc, -1, v131
	v_add_u32_e32 v174, v157, v161
	ds_read_b128 v[170:173], v174
	s_and_saveexec_b64 s[4:5], vcc
	s_cbranch_execz .LBB0_944
	v_add_u32_e32 v133, v157, v159
	ds_read_b128 v[166:169], v133
	v_lshrrev_b32_e32 v133, 8, v131
	v_mul_u32_u24_e32 v133, s2, v133
	v_lshlrev_b32_e32 v131, 7, v131
	v_add_lshl_u32 v133, v133, s6, 15
	v_and_b32_e32 v131, 0x7f80, v131
	v_add3_u32 v131, v131, v132, v133
	s_waitcnt lgkmcnt(0)
	global_store_dwordx4 v131, v[166:169], s[50:51]
.LBB0_944:
	s_or_b64 exec, exec, s[4:5]
	v_add_u32_e32 v131, s19, v160
	v_cmp_lt_i32_e32 vcc, -1, v131
	s_and_saveexec_b64 s[4:5], vcc
	s_cbranch_execz .LBB0_801
	v_add_u32_e32 v133, v157, v161
	v_lshrrev_b32_e32 v133, 8, v131
	v_mul_u32_u24_e32 v133, s2, v133
	v_lshlrev_b32_e32 v131, 7, v131
	v_add_lshl_u32 v133, v133, s6, 15
	v_and_b32_e32 v131, 0x7f80, v131
	v_add3_u32 v131, v131, v132, v133
	s_waitcnt lgkmcnt(0)
	global_store_dwordx4 v131, v[170:173], s[50:51]
	s_branch .LBB0_801

; #define GAS __attribute__((address_space(1)))
; #define LAS __attribute__((address_space(3)))
; #define LDS_BARRIER() do { asm volatile("s_waitcnt lgkmcnt(0)" ::: "memory"); __builtin_amdgcn_s_barrier(); asm volatile("" ::: "memory"); } while (0)
; __device__ __forceinline__ unsigned pk4_fp8(float a, float b, float c, float d) {
;     a = __builtin_amdgcn_fmed3f(a, -448.f, 448.f); b = __builtin_amdgcn_fmed3f(b, -448.f, 448.f); c = __builtin_amdgcn_fmed3f(c, -448.f, 448.f); d = __builtin_amdgcn_fmed3f(d, -448.f, 448.f);
;     int w = 0; w = __builtin_amdgcn_cvt_pk_fp8_f32(a, b, w, false); w = __builtin_amdgcn_cvt_pk_fp8_f32(c, d, w, true); return (unsigned)w; }
; template <class RowMap>
; __device__ __forceinline__ void conv_store_fp8(const f32x4 (&r)[8], unsigned char* WT, int Kbytes, int k0bytes, int n0, const RowMap rm, LAS unsigned char* T, int tid, int wave, int lane) {
;     const int s = 2 * (lane & 3);
; #pragma unroll
;     for (int j = 0; j < 4; ++j) { const unsigned lo = pk4_fp8(r[0][j] * W8_SCALE, r[1][j] * W8_SCALE, r[2][j] * W8_SCALE, r[3][j] * W8_SCALE), hi = pk4_fp8(r[4][j] * W8_SCALE, r[5][j] * W8_SCALE, r[6][j] * W8_SCALE, r[7][j] * W8_SCALE);
;         *(LAS unsigned long long*)(T + (4 * lane + j) * 64 + 8 * (wave ^ s)) = (unsigned long long)lo | ((unsigned long long)hi << 32); }
;     LDS_BARRIER();
;     const int c16 = tid & 3, rr = tid >> 2;
; #pragma unroll
;     for (int q = 0; q < 2; ++q) { const int row = rr + 128 * q; const v4u v = *(const LAS v4u*)(T + row * 64 + 16 * (c16 ^ ((row >> 2) & 3)));
;         const int dr = rm(n0 + row); if (dr >= 0) *(GAS v4u*)(WT + (unsigned)((((dr >> 8) * (Kbytes >> 7) + (k0bytes >> 7)) << 15) + ((dr & 255) << 7) + (k0bytes & 127) + 16 * c16)) = v; }
;     LDS_BARRIER();
; }
.Lhw_done_7:
	v_med3_f32 v131, v2, s101, v200
	v_med3_f32 v153, v6, s101, v200
	v_mov_b32_e32 v132, v130
	v_cvt_scalef32_pk_fp8_f32 v132, v131, v153, v201
	v_med3_f32 v133, v10, s101, v200
	v_med3_f32 v152, v14, s101, v200
	v_cvt_scalef32_pk_fp8_f32 v132, v133, v152, v201 op_sel:[0,0,0,1]
	v_med3_f32 v131, v18, s101, v200
	v_med3_f32 v158, v22, s101, v200
	v_mov_b32_e32 v133, v130
	v_cvt_scalef32_pk_fp8_f32 v133, v131, v158, v201
	v_med3_f32 v152, v50, s101, v200
	v_med3_f32 v153, v54, s101, v200
	v_cvt_scalef32_pk_fp8_f32 v133, v152, v153, v201 op_sel:[0,0,0,1]
	v_med3_f32 v131, v3, s101, v200
	v_med3_f32 v159, v7, s101, v200
	v_mov_b32_e32 v152, v130
	v_cvt_scalef32_pk_fp8_f32 v152, v131, v159, v201
	v_med3_f32 v153, v11, s101, v200
	v_med3_f32 v158, v15, s101, v200
	v_cvt_scalef32_pk_fp8_f32 v152, v153, v158, v201 op_sel:[0,0,0,1]
	v_med3_f32 v131, v19, s101, v200
	v_med3_f32 v172, v23, s101, v200
	v_mov_b32_e32 v153, v130
	v_cvt_scalef32_pk_fp8_f32 v153, v131, v172, v201
	v_med3_f32 v158, v51, s101, v200
	v_med3_f32 v159, v55, s101, v200
	v_cvt_scalef32_pk_fp8_f32 v153, v158, v159, v201 op_sel:[0,0,0,1]
	v_med3_f32 v131, v4, s101, v200
	s_cmp_lg_u32 s12, 0
	ds_write2_b64 v171, v[132:133], v[152:153] offset1:8
	v_med3_f32 v153, v8, s101, v200
	v_mov_b32_e32 v132, v130
	v_cvt_scalef32_pk_fp8_f32 v132, v131, v153, v201
	v_med3_f32 v133, v12, s101, v200
	v_med3_f32 v152, v16, s101, v200
	v_cvt_scalef32_pk_fp8_f32 v132, v133, v152, v201 op_sel:[0,0,0,1]
	v_med3_f32 v131, v20, s101, v200
	v_med3_f32 v158, v24, s101, v200
	v_mov_b32_e32 v133, v130
	v_cvt_scalef32_pk_fp8_f32 v133, v131, v158, v201
	v_med3_f32 v152, v52, s101, v200
	v_med3_f32 v153, v56, s101, v200
	v_cvt_scalef32_pk_fp8_f32 v133, v152, v153, v201 op_sel:[0,0,0,1]
	v_med3_f32 v131, v5, s101, v200
	v_med3_f32 v159, v9, s101, v200
	v_mov_b32_e32 v152, v130
	v_cvt_scalef32_pk_fp8_f32 v152, v131, v159, v201
	v_med3_f32 v153, v13, s101, v200
	v_med3_f32 v158, v17, s101, v200
	v_cvt_scalef32_pk_fp8_f32 v152, v153, v158, v201 op_sel:[0,0,0,1]
	v_med3_f32 v131, v21, s101, v200
	v_med3_f32 v172, v25, s101, v200
	v_mov_b32_e32 v153, v130
	v_cvt_scalef32_pk_fp8_f32 v153, v131, v172, v201
	v_med3_f32 v158, v53, s101, v200
	v_med3_f32 v159, v57, s101, v200
	v_cvt_scalef32_pk_fp8_f32 v153, v158, v159, v201 op_sel:[0,0,0,1]
	ds_write2_b64 v171, v[132:133], v[152:153] offset0:16 offset1:24
	s_cbranch_scc0 .LBB0_2350
	s_lshl_b32 s12, s12, 7
	v_add_lshl_u32 v132, s24, v160, 1
	s_waitcnt lgkmcnt(0)
	s_barrier
	s_add_i32 s47, s12, 0xffffff00
	v_and_b32_e32 v132, 0xffffff00, v132
	s_and_b32 s13, s33, 0x7f
	v_add_u32_e32 v133, s47, v132
	v_or_b32_e32 v132, s12, v166
	s_lshr_b32 s37, s33, 7
	v_add_u32_e32 v131, s13, v162
	v_cmp_lt_i32_e32 vcc, -1, v133
	v_lshlrev_b32_e32 v132, 7, v132
	v_add_u32_e32 v180, v161, v165
	ds_read_b128 v[176:179], v180
	s_and_saveexec_b64 s[12:13], vcc
	s_cbranch_execz .LBB0_2339
	v_add_u32_e32 v152, v161, v163
	ds_read_b128 v[172:175], v152
	v_lshrrev_b32_e32 v133, 8, v133
	v_mul_u32_u24_e32 v133, s26, v133
	v_add_lshl_u32 v133, v133, s37, 15
	v_and_b32_e32 v152, 0x7f80, v132
	v_add3_u32 v133, v152, v131, v133
	s_waitcnt lgkmcnt(0)
	global_store_dwordx4 v133, v[172:175], s[6:7]
.LBB0_2339:
	s_or_b64 exec, exec, s[12:13]
	v_add_lshl_u32 v133, s24, v164, 1
	v_and_b32_e32 v133, 0xffffff00, v133
	v_add_u32_e32 v133, s47, v133
	v_cmp_lt_i32_e32 vcc, -1, v133
	s_and_saveexec_b64 s[12:13], vcc
	s_cbranch_execz .LBB0_2341
	v_add_u32_e32 v152, v161, v165
	v_lshrrev_b32_e32 v133, 8, v133
	v_mul_u32_u24_e32 v133, s26, v133
	v_add_lshl_u32 v133, v133, s37, 15
	v_and_b32_e32 v132, 0x7f80, v132
	v_add3_u32 v131, v132, v131, v133
	s_waitcnt lgkmcnt(0)
	global_store_dwordx4 v131, v[176:179], s[6:7]

; #define GAS __attribute__((address_space(1)))
; #define LAS __attribute__((address_space(3)))
; #define LDS_BARRIER() do { asm volatile("s_waitcnt lgkmcnt(0)" ::: "memory"); __builtin_amdgcn_s_barrier(); asm volatile("" ::: "memory"); } while (0)
; template <class RowMap>
; __device__ __forceinline__ void conv_store_fp8(const f32x4 (&r)[8], unsigned char* WT, int Kbytes, int k0bytes, int n0, const RowMap rm, LAS unsigned char* T, int tid, int wave, int lane) {
;     ...
;     const int c16 = tid & 3, rr = tid >> 2;
; #pragma unroll
;     for (int q = 0; q < 2; ++q) { const int row = rr + 128 * q; const v4u v = *(const LAS v4u*)(T + row * 64 + 16 * (c16 ^ ((row >> 2) & 3)));
;         const int dr = rm(n0 + row); if (dr >= 0) *(GAS v4u*)(WT + (unsigned)((((dr >> 8) * (Kbytes >> 7) + (k0bytes >> 7)) << 15) + ((dr & 255) << 7) + (k0bytes & 127) + 16 * c16)) = v; }
;     LDS_BARRIER();
.LBB0_2342:
	s_waitcnt lgkmcnt(0)
	s_barrier
	s_and_b32 s12, s33, 0x7f
	v_add_u32_e32 v132, s24, v160
	s_lshr_b32 s37, s33, 7
	v_add_u32_e32 v131, s12, v162
	v_cmp_lt_i32_e32 vcc, -1, v132
	v_add_u32_e32 v180, v161, v165
	ds_read_b128 v[176:179], v180
	s_and_saveexec_b64 s[12:13], vcc
	s_cbranch_execz .LBB0_2344
	v_add_u32_e32 v133, v161, v163
	ds_read_b128 v[172:175], v133
	v_lshrrev_b32_e32 v132, 8, v132
	v_mul_u32_u24_e32 v132, s26, v132
	v_add_lshl_u32 v132, v132, s37, 15
	v_add3_u32 v132, v131, v167, v132
	s_waitcnt lgkmcnt(0)
	global_store_dwordx4 v132, v[172:175], s[6:7]
.LBB0_2344:
	s_or_b64 exec, exec, s[12:13]
	v_add_u32_e32 v132, s24, v164
	v_cmp_lt_i32_e32 vcc, -1, v132
	s_and_saveexec_b64 s[12:13], vcc
	s_cbranch_execz .LBB0_2346
	v_add_u32_e32 v133, v161, v165
	v_lshrrev_b32_e32 v132, 8, v132
	v_mul_u32_u24_e32 v132, s26, v132
	v_add_lshl_u32 v132, v132, s37, 15
	v_add3_u32 v131, v131, v168, v132
	s_waitcnt lgkmcnt(0)
	global_store_dwordx4 v131, v[176:179], s[6:7]

; #define GAS __attribute__((address_space(1)))
; #define LAS __attribute__((address_space(3)))
; #define LDS_BARRIER() do { asm volatile("s_waitcnt lgkmcnt(0)" ::: "memory"); __builtin_amdgcn_s_barrier(); asm volatile("" ::: "memory"); } while (0)
; __device__ __forceinline__ unsigned pk4_fp8(float a, float b, float c, float d) {
;     a = __builtin_amdgcn_fmed3f(a, -448.f, 448.f); b = __builtin_amdgcn_fmed3f(b, -448.f, 448.f); c = __builtin_amdgcn_fmed3f(c, -448.f, 448.f); d = __builtin_amdgcn_fmed3f(d, -448.f, 448.f);
;     int w = 0; w = __builtin_amdgcn_cvt_pk_fp8_f32(a, b, w, false); w = __builtin_amdgcn_cvt_pk_fp8_f32(c, d, w, true); return (unsigned)w; }
; template <class RowMap>
; __device__ __forceinline__ void conv_store_fp8(const f32x4 (&r)[8], unsigned char* WT, int Kbytes, int k0bytes, int n0, const RowMap rm, LAS unsigned char* T, int tid, int wave, int lane) {
;     const int s = 2 * (lane & 3);
; #pragma unroll
;     for (int j = 0; j < 4; ++j) { const unsigned lo = pk4_fp8(r[0][j] * W8_SCALE, r[1][j] * W8_SCALE, r[2][j] * W8_SCALE, r[3][j] * W8_SCALE), hi = pk4_fp8(r[4][j] * W8_SCALE, r[5][j] * W8_SCALE, r[6][j] * W8_SCALE, r[7][j] * W8_SCALE);
;         *(LAS unsigned long long*)(T + (4 * lane + j) * 64 + 8 * (wave ^ s)) = (unsigned long long)lo | ((unsigned long long)hi << 32); }
;     LDS_BARRIER();
;     const int c16 = tid & 3, rr = tid >> 2;
; #pragma unroll
;     for (int q = 0; q < 2; ++q) { const int row = rr + 128 * q; const v4u v = *(const LAS v4u*)(T + row * 64 + 16 * (c16 ^ ((row >> 2) & 3)));
;         const int dr = rm(n0 + row); if (dr >= 0) *(GAS v4u*)(WT + (unsigned)((((dr >> 8) * (Kbytes >> 7) + (k0bytes >> 7)) << 15) + ((dr & 255) << 7) + (k0bytes & 127) + 16 * c16)) = v; }
;     LDS_BARRIER();
; }
.Lhw_done_8:
	v_med3_f32 v131, v26, s101, v200
	v_med3_f32 v153, v30, s101, v200
	v_mov_b32_e32 v132, v130
	v_cvt_scalef32_pk_fp8_f32 v132, v131, v153, v201
	v_med3_f32 v133, v34, s101, v200
	v_med3_f32 v152, v38, s101, v200
	v_cvt_scalef32_pk_fp8_f32 v132, v133, v152, v201 op_sel:[0,0,0,1]
	v_med3_f32 v131, v42, s101, v200
	v_med3_f32 v158, v46, s101, v200
	v_mov_b32_e32 v133, v130
	v_cvt_scalef32_pk_fp8_f32 v133, v131, v158, v201
	v_med3_f32 v152, v66, s101, v200
	v_med3_f32 v153, v70, s101, v200
	v_cvt_scalef32_pk_fp8_f32 v133, v152, v153, v201 op_sel:[0,0,0,1]
	v_med3_f32 v131, v27, s101, v200
	v_med3_f32 v159, v31, s101, v200
	v_mov_b32_e32 v152, v130
	v_cvt_scalef32_pk_fp8_f32 v152, v131, v159, v201
	v_med3_f32 v153, v35, s101, v200
	v_med3_f32 v158, v39, s101, v200
	v_cvt_scalef32_pk_fp8_f32 v152, v153, v158, v201 op_sel:[0,0,0,1]
	v_med3_f32 v131, v43, s101, v200
	v_med3_f32 v172, v47, s101, v200
	v_mov_b32_e32 v153, v130
	v_cvt_scalef32_pk_fp8_f32 v153, v131, v172, v201
	v_med3_f32 v158, v67, s101, v200
	v_med3_f32 v159, v71, s101, v200
	v_cvt_scalef32_pk_fp8_f32 v153, v158, v159, v201 op_sel:[0,0,0,1]
	v_med3_f32 v131, v28, s101, v200
	s_cmp_lg_u32 s12, 0
	ds_write2_b64 v171, v[132:133], v[152:153] offset1:8
	v_med3_f32 v153, v32, s101, v200
	v_mov_b32_e32 v132, v130
	v_cvt_scalef32_pk_fp8_f32 v132, v131, v153, v201
	v_med3_f32 v133, v36, s101, v200
	v_med3_f32 v152, v40, s101, v200
	v_cvt_scalef32_pk_fp8_f32 v132, v133, v152, v201 op_sel:[0,0,0,1]
	v_med3_f32 v131, v44, s101, v200
	v_med3_f32 v158, v48, s101, v200
	v_mov_b32_e32 v133, v130
	v_cvt_scalef32_pk_fp8_f32 v133, v131, v158, v201
	v_med3_f32 v152, v68, s101, v200
	v_med3_f32 v153, v72, s101, v200
	v_cvt_scalef32_pk_fp8_f32 v133, v152, v153, v201 op_sel:[0,0,0,1]
	v_med3_f32 v131, v29, s101, v200
	v_med3_f32 v159, v33, s101, v200
	v_mov_b32_e32 v152, v130
	v_cvt_scalef32_pk_fp8_f32 v152, v131, v159, v201
	v_med3_f32 v153, v37, s101, v200
	v_med3_f32 v158, v41, s101, v200
	v_cvt_scalef32_pk_fp8_f32 v152, v153, v158, v201 op_sel:[0,0,0,1]
	v_med3_f32 v131, v45, s101, v200
	v_med3_f32 v172, v49, s101, v200
	v_mov_b32_e32 v153, v130
	v_cvt_scalef32_pk_fp8_f32 v153, v131, v172, v201
	v_med3_f32 v158, v69, s101, v200
	v_med3_f32 v159, v73, s101, v200
	v_cvt_scalef32_pk_fp8_f32 v153, v158, v159, v201 op_sel:[0,0,0,1]
	ds_write2_b64 v171, v[132:133], v[152:153] offset0:16 offset1:24
	s_cbranch_scc0 .LBB0_2375
	s_lshl_b32 s12, s12, 7
	v_add_lshl_u32 v132, s24, v160, 1
	s_waitcnt lgkmcnt(0)
	s_barrier
	s_add_i32 s47, s12, 0xffffff00
	v_and_b32_e32 v132, 0xffffff00, v132
	s_and_b32 s13, s33, 0x7f
	v_add_u32_e32 v133, s47, v132
	v_or_b32_e32 v132, s12, v166
	s_lshr_b32 s37, s33, 7
	v_add_u32_e32 v131, s13, v162
	v_cmp_lt_i32_e32 vcc, -1, v133
	v_lshlrev_b32_e32 v132, 7, v132
	v_add_u32_e32 v180, v161, v165
	ds_read_b128 v[176:179], v180
	s_and_saveexec_b64 s[12:13], vcc
	s_cbranch_execz .LBB0_2372
	v_add_u32_e32 v152, v161, v163
	ds_read_b128 v[172:175], v152
	v_lshrrev_b32_e32 v133, 8, v133
	v_mul_u32_u24_e32 v133, s26, v133
	v_add_lshl_u32 v133, v133, s37, 15
	v_and_b32_e32 v152, 0x7f80, v132
	v_add3_u32 v133, v152, v131, v133
	s_waitcnt lgkmcnt(0)
	global_store_dwordx4 v133, v[172:175], s[6:7]

; #define GAS __attribute__((address_space(1)))
; #define LAS __attribute__((address_space(3)))
; #define LDS_BARRIER() do { asm volatile("s_waitcnt lgkmcnt(0)" ::: "memory"); __builtin_amdgcn_s_barrier(); asm volatile("" ::: "memory"); } while (0)
; template <class RowMap>
; __device__ __forceinline__ void conv_store_fp8(const f32x4 (&r)[8], unsigned char* WT, int Kbytes, int k0bytes, int n0, const RowMap rm, LAS unsigned char* T, int tid, int wave, int lane) {
;     ...
;     const int c16 = tid & 3, rr = tid >> 2;
; #pragma unroll
;     for (int q = 0; q < 2; ++q) { const int row = rr + 128 * q; const v4u v = *(const LAS v4u*)(T + row * 64 + 16 * (c16 ^ ((row >> 2) & 3)));
;         const int dr = rm(n0 + row); if (dr >= 0) *(GAS v4u*)(WT + (unsigned)((((dr >> 8) * (Kbytes >> 7) + (k0bytes >> 7)) << 15) + ((dr & 255) << 7) + (k0bytes & 127) + 16 * c16)) = v; }
;     LDS_BARRIER();
.LBB0_2375:
	s_cbranch_execz .LBB0_2381
	s_waitcnt lgkmcnt(0)
	s_barrier
	s_and_b32 s12, s33, 0x7f
	v_add_u32_e32 v132, s24, v160
	s_lshr_b32 s37, s33, 7
	v_add_u32_e32 v131, s12, v162
	v_cmp_lt_i32_e32 vcc, -1, v132
	v_add_u32_e32 v180, v161, v165
	ds_read_b128 v[176:179], v180
	s_and_saveexec_b64 s[12:13], vcc
	s_cbranch_execz .LBB0_2378
	v_add_u32_e32 v133, v161, v163
	ds_read_b128 v[172:175], v133
	v_lshrrev_b32_e32 v132, 8, v132
	v_mul_u32_u24_e32 v132, s26, v132
	v_add_lshl_u32 v132, v132, s37, 15
	v_add3_u32 v132, v131, v167, v132
	s_waitcnt lgkmcnt(0)
	global_store_dwordx4 v132, v[172:175], s[6:7]

; #define GAS __attribute__((address_space(1)))
; #define LAS __attribute__((address_space(3)))
; #define LDS_BARRIER() do { asm volatile("s_waitcnt lgkmcnt(0)" ::: "memory"); __builtin_amdgcn_s_barrier(); asm volatile("" ::: "memory"); } while (0)
; __device__ __forceinline__ unsigned pk4_fp8(float a, float b, float c, float d) {
;     a = __builtin_amdgcn_fmed3f(a, -448.f, 448.f); b = __builtin_amdgcn_fmed3f(b, -448.f, 448.f); c = __builtin_amdgcn_fmed3f(c, -448.f, 448.f); d = __builtin_amdgcn_fmed3f(d, -448.f, 448.f);
;     int w = 0; w = __builtin_amdgcn_cvt_pk_fp8_f32(a, b, w, false); w = __builtin_amdgcn_cvt_pk_fp8_f32(c, d, w, true); return (unsigned)w; }
; template <class RowMap>
; __device__ __forceinline__ void conv_store_fp8(const f32x4 (&r)[8], unsigned char* WT, int Kbytes, int k0bytes, int n0, const RowMap rm, LAS unsigned char* T, int tid, int wave, int lane) {
;     const int s = 2 * (lane & 3);
; #pragma unroll
;     for (int j = 0; j < 4; ++j) { const unsigned lo = pk4_fp8(r[0][j] * W8_SCALE, r[1][j] * W8_SCALE, r[2][j] * W8_SCALE, r[3][j] * W8_SCALE), hi = pk4_fp8(r[4][j] * W8_SCALE, r[5][j] * W8_SCALE, r[6][j] * W8_SCALE, r[7][j] * W8_SCALE);
;         *(LAS unsigned long long*)(T + (4 * lane + j) * 64 + 8 * (wave ^ s)) = (unsigned long long)lo | ((unsigned long long)hi << 32); }
;     LDS_BARRIER();
;     const int c16 = tid & 3, rr = tid >> 2;
; #pragma unroll
;     for (int q = 0; q < 2; ++q) { const int row = rr + 128 * q; const v4u v = *(const LAS v4u*)(T + row * 64 + 16 * (c16 ^ ((row >> 2) & 3)));
;         const int dr = rm(n0 + row); if (dr >= 0) *(GAS v4u*)(WT + (unsigned)((((dr >> 8) * (Kbytes >> 7) + (k0bytes >> 7)) << 15) + ((dr & 255) << 7) + (k0bytes & 127) + 16 * c16)) = v; }
;     LDS_BARRIER();
; }
.Lhw_done_9:
	v_med3_f32 v131, v58, s101, v200
	v_med3_f32 v153, v62, s101, v200
	v_mov_b32_e32 v132, v130
	v_cvt_scalef32_pk_fp8_f32 v132, v131, v153, v201
	v_med3_f32 v133, v74, s101, v200
	v_med3_f32 v152, v78, s101, v200
	v_cvt_scalef32_pk_fp8_f32 v132, v133, v152, v201 op_sel:[0,0,0,1]
	v_med3_f32 v131, v82, s101, v200
	v_med3_f32 v158, v86, s101, v200
	v_mov_b32_e32 v133, v130
	v_cvt_scalef32_pk_fp8_f32 v133, v131, v158, v201
	v_med3_f32 v152, v102, s101, v200
	v_med3_f32 v153, v106, s101, v200
	v_cvt_scalef32_pk_fp8_f32 v133, v152, v153, v201 op_sel:[0,0,0,1]
	v_med3_f32 v131, v59, s101, v200
	v_med3_f32 v159, v63, s101, v200
	v_mov_b32_e32 v152, v130
	v_cvt_scalef32_pk_fp8_f32 v152, v131, v159, v201
	v_med3_f32 v153, v75, s101, v200
	v_med3_f32 v158, v79, s101, v200
	v_cvt_scalef32_pk_fp8_f32 v152, v153, v158, v201 op_sel:[0,0,0,1]
	v_med3_f32 v131, v83, s101, v200
	v_med3_f32 v172, v87, s101, v200
	v_mov_b32_e32 v153, v130
	v_cvt_scalef32_pk_fp8_f32 v153, v131, v172, v201
	v_med3_f32 v158, v103, s101, v200
	v_med3_f32 v159, v107, s101, v200
	v_cvt_scalef32_pk_fp8_f32 v153, v158, v159, v201 op_sel:[0,0,0,1]
	v_med3_f32 v131, v60, s101, v200
	s_cmp_lg_u32 s12, 0
	ds_write2_b64 v171, v[132:133], v[152:153] offset1:8
	v_med3_f32 v153, v64, s101, v200
	v_mov_b32_e32 v132, v130
	v_cvt_scalef32_pk_fp8_f32 v132, v131, v153, v201
	v_med3_f32 v133, v76, s101, v200
	v_med3_f32 v152, v80, s101, v200
	v_cvt_scalef32_pk_fp8_f32 v132, v133, v152, v201 op_sel:[0,0,0,1]
	v_med3_f32 v131, v84, s101, v200
	v_med3_f32 v158, v88, s101, v200
	v_mov_b32_e32 v133, v130
	v_cvt_scalef32_pk_fp8_f32 v133, v131, v158, v201
	v_med3_f32 v152, v104, s101, v200
	v_med3_f32 v153, v108, s101, v200
	v_cvt_scalef32_pk_fp8_f32 v133, v152, v153, v201 op_sel:[0,0,0,1]
	v_med3_f32 v131, v61, s101, v200
	v_med3_f32 v159, v65, s101, v200
	v_mov_b32_e32 v152, v130
	v_cvt_scalef32_pk_fp8_f32 v152, v131, v159, v201
	v_med3_f32 v153, v77, s101, v200
	v_med3_f32 v158, v81, s101, v200
	v_cvt_scalef32_pk_fp8_f32 v152, v153, v158, v201 op_sel:[0,0,0,1]
	v_med3_f32 v131, v85, s101, v200
	v_med3_f32 v172, v89, s101, v200
	v_mov_b32_e32 v153, v130
	v_cvt_scalef32_pk_fp8_f32 v153, v131, v172, v201
	v_med3_f32 v158, v105, s101, v200
	v_med3_f32 v159, v109, s101, v200
	v_cvt_scalef32_pk_fp8_f32 v153, v158, v159, v201 op_sel:[0,0,0,1]
	ds_write2_b64 v171, v[132:133], v[152:153] offset0:16 offset1:24
	s_cbranch_scc0 .LBB0_2407
	s_lshl_b32 s12, s12, 7
	v_add_lshl_u32 v132, s24, v160, 1
	s_waitcnt lgkmcnt(0)
	s_barrier
	s_add_i32 s47, s12, 0xffffff00
	v_and_b32_e32 v132, 0xffffff00, v132
	s_and_b32 s13, s33, 0x7f
	v_add_u32_e32 v133, s47, v132
	v_or_b32_e32 v132, s12, v166
	s_lshr_b32 s37, s33, 7
	v_add_u32_e32 v131, s13, v162
	v_cmp_lt_i32_e32 vcc, -1, v133
	v_lshlrev_b32_e32 v132, 7, v132
	v_add_u32_e32 v180, v161, v165
	ds_read_b128 v[176:179], v180
	s_and_saveexec_b64 s[12:13], vcc
	s_cbranch_execz .LBB0_2404
	v_add_u32_e32 v152, v161, v163
	ds_read_b128 v[172:175], v152
	v_lshrrev_b32_e32 v133, 8, v133
	v_mul_u32_u24_e32 v133, s26, v133
	v_add_lshl_u32 v133, v133, s37, 15
	v_and_b32_e32 v152, 0x7f80, v132
	v_add3_u32 v133, v152, v131, v133
	s_waitcnt lgkmcnt(0)
	global_store_dwordx4 v133, v[172:175], s[6:7]

; #define GAS __attribute__((address_space(1)))
; #define LAS __attribute__((address_space(3)))
; #define LDS_BARRIER() do { asm volatile("s_waitcnt lgkmcnt(0)" ::: "memory"); __builtin_amdgcn_s_barrier(); asm volatile("" ::: "memory"); } while (0)
; template <class RowMap>
; __device__ __forceinline__ void conv_store_fp8(const f32x4 (&r)[8], unsigned char* WT, int Kbytes, int k0bytes, int n0, const RowMap rm, LAS unsigned char* T, int tid, int wave, int lane) {
;     ...
;     for (int j = 0; j < 4; ++j) { const unsigned lo = pk4_fp8(r[0][j] * W8_SCALE, r[1][j] * W8_SCALE, r[2][j] * W8_SCALE, r[3][j] * W8_SCALE), hi = pk4_fp8(r[4][j] * W8_SCALE, r[5][j] * W8_SCALE, r[6][j] * W8_SCALE, r[7][j] * W8_SCALE);
;         *(LAS unsigned long long*)(T + (4 * lane + j) * 64 + 8 * (wave ^ s)) = (unsigned long long)lo | ((unsigned long long)hi << 32); }
;     LDS_BARRIER();
;     const int c16 = tid & 3, rr = tid >> 2;
; #pragma unroll
;     for (int q = 0; q < 2; ++q) { const int row = rr + 128 * q; const v4u v = *(const LAS v4u*)(T + row * 64 + 16 * (c16 ^ ((row >> 2) & 3)));
;         const int dr = rm(n0 + row); if (dr >= 0) *(GAS v4u*)(WT + (unsigned)((((dr >> 8) * (Kbytes >> 7) + (k0bytes >> 7)) << 15) + ((dr & 255) << 7) + (k0bytes & 127) + 16 * c16)) = v; }
.Lhw_done_10:
	v_med3_f32 v131, v94, s101, v200
	v_med3_f32 v153, v98, s101, v200
	v_mov_b32_e32 v132, v130
	v_cvt_scalef32_pk_fp8_f32 v132, v131, v153, v201
	v_med3_f32 v133, v90, s101, v200
	v_med3_f32 v152, v110, s101, v200
	v_cvt_scalef32_pk_fp8_f32 v132, v133, v152, v201 op_sel:[0,0,0,1]
	v_med3_f32 v131, v114, s101, v200
	v_med3_f32 v158, v118, s101, v200
	v_mov_b32_e32 v133, v130
	v_cvt_scalef32_pk_fp8_f32 v133, v131, v158, v201
	v_med3_f32 v152, v126, s101, v200
	v_med3_f32 v153, v122, s101, v200
	v_cvt_scalef32_pk_fp8_f32 v133, v152, v153, v201 op_sel:[0,0,0,1]
	v_med3_f32 v131, v95, s101, v200
	v_med3_f32 v159, v99, s101, v200
	v_mov_b32_e32 v152, v130
	v_cvt_scalef32_pk_fp8_f32 v152, v131, v159, v201
	v_med3_f32 v153, v91, s101, v200
	v_med3_f32 v158, v111, s101, v200
	v_cvt_scalef32_pk_fp8_f32 v152, v153, v158, v201 op_sel:[0,0,0,1]
	v_med3_f32 v131, v115, s101, v200
	v_med3_f32 v172, v119, s101, v200
	v_mov_b32_e32 v153, v130
	v_cvt_scalef32_pk_fp8_f32 v153, v131, v172, v201
	v_med3_f32 v158, v127, s101, v200
	v_med3_f32 v159, v123, s101, v200
	v_cvt_scalef32_pk_fp8_f32 v153, v158, v159, v201 op_sel:[0,0,0,1]
	v_med3_f32 v131, v96, s101, v200
	s_cmp_lg_u32 s6, 0
	ds_write2_b64 v171, v[132:133], v[152:153] offset1:8
	v_med3_f32 v153, v100, s101, v200
	v_mov_b32_e32 v132, v130
	v_cvt_scalef32_pk_fp8_f32 v132, v131, v153, v201
	v_med3_f32 v133, v92, s101, v200
	v_med3_f32 v152, v112, s101, v200
	v_cvt_scalef32_pk_fp8_f32 v132, v133, v152, v201 op_sel:[0,0,0,1]
	v_med3_f32 v131, v116, s101, v200
	v_med3_f32 v158, v120, s101, v200
	v_mov_b32_e32 v133, v130
	v_cvt_scalef32_pk_fp8_f32 v133, v131, v158, v201
	v_med3_f32 v152, v128, s101, v200
	v_med3_f32 v153, v124, s101, v200
	v_cvt_scalef32_pk_fp8_f32 v133, v152, v153, v201 op_sel:[0,0,0,1]
	v_med3_f32 v131, v97, s101, v200
	v_med3_f32 v159, v101, s101, v200
	v_mov_b32_e32 v152, v130
	v_cvt_scalef32_pk_fp8_f32 v152, v131, v159, v201
	v_med3_f32 v153, v93, s101, v200
	v_med3_f32 v158, v113, s101, v200
	v_cvt_scalef32_pk_fp8_f32 v152, v153, v158, v201 op_sel:[0,0,0,1]
	v_med3_f32 v131, v117, s101, v200
	v_med3_f32 v172, v121, s101, v200
	v_mov_b32_e32 v153, v130
	v_cvt_scalef32_pk_fp8_f32 v153, v131, v172, v201
	v_med3_f32 v158, v129, s101, v200
	v_med3_f32 v159, v125, s101, v200
	v_cvt_scalef32_pk_fp8_f32 v153, v158, v159, v201 op_sel:[0,0,0,1]
	ds_write2_b64 v171, v[132:133], v[152:153] offset0:16 offset1:24
	s_cbranch_scc0 .LBB0_2439
	s_lshl_b32 s6, s6, 7
	v_add_lshl_u32 v132, s2, v160, 1
	s_waitcnt lgkmcnt(0)
	s_barrier
	s_add_i32 s24, s6, 0xffffff00
	v_and_b32_e32 v132, 0xffffff00, v132
	s_and_b32 s7, s13, 0x7f
	v_add_u32_e32 v133, s24, v132
	v_or_b32_e32 v132, s6, v166
	s_lshr_b32 s18, s13, 7
	v_add_u32_e32 v131, s7, v162
	v_cmp_lt_i32_e32 vcc, -1, v133
	v_lshlrev_b32_e32 v132, 7, v132
	v_add_u32_e32 v180, v161, v165
	ds_read_b128 v[176:179], v180
	s_and_saveexec_b64 s[6:7], vcc
	s_cbranch_execz .LBB0_2436
	v_add_u32_e32 v152, v161, v163
	ds_read_b128 v[172:175], v152
	v_lshrrev_b32_e32 v133, 8, v133
	v_mul_u32_u24_e32 v133, s12, v133
	v_add_lshl_u32 v133, v133, s18, 15
	v_and_b32_e32 v152, 0x7f80, v132
	v_add3_u32 v133, v152, v131, v133
	s_waitcnt lgkmcnt(0)
	global_store_dwordx4 v133, v[172:175], s[4:5]
.LBB0_2436:
	s_or_b64 exec, exec, s[6:7]
	v_add_lshl_u32 v133, s2, v164, 1
	v_and_b32_e32 v133, 0xffffff00, v133
	v_add_u32_e32 v133, s24, v133
	v_cmp_lt_i32_e32 vcc, -1, v133
	s_and_saveexec_b64 s[6:7], vcc
	s_cbranch_execz .LBB0_2438
	v_add_u32_e32 v152, v161, v165
	v_lshrrev_b32_e32 v133, 8, v133
	v_mul_u32_u24_e32 v133, s12, v133
	v_add_lshl_u32 v133, v133, s18, 15
	v_and_b32_e32 v132, 0x7f80, v132
	v_add3_u32 v131, v132, v131, v133
	s_waitcnt lgkmcnt(0)
	global_store_dwordx4 v131, v[176:179], s[4:5]

; #define GAS __attribute__((address_space(1)))
; #define LAS __attribute__((address_space(3)))
; #define LDS_BARRIER() do { asm volatile("s_waitcnt lgkmcnt(0)" ::: "memory"); __builtin_amdgcn_s_barrier(); asm volatile("" ::: "memory"); } while (0)
; template <class RowMap>
; __device__ __forceinline__ void conv_store_fp8(const f32x4 (&r)[8], unsigned char* WT, int Kbytes, int k0bytes, int n0, const RowMap rm, LAS unsigned char* T, int tid, int wave, int lane) {
;     ...
;     const int c16 = tid & 3, rr = tid >> 2;
; #pragma unroll
;     for (int q = 0; q < 2; ++q) { const int row = rr + 128 * q; const v4u v = *(const LAS v4u*)(T + row * 64 + 16 * (c16 ^ ((row >> 2) & 3)));
;         const int dr = rm(n0 + row); if (dr >= 0) *(GAS v4u*)(WT + (unsigned)((((dr >> 8) * (Kbytes >> 7) + (k0bytes >> 7)) << 15) + ((dr & 255) << 7) + (k0bytes & 127) + 16 * c16)) = v; }
;     LDS_BARRIER();
.LBB0_2439:
	s_cbranch_execz .LBB0_2314
	s_waitcnt lgkmcnt(0)
	s_barrier
	s_and_b32 s6, s13, 0x7f
	v_add_u32_e32 v132, s2, v160
	s_lshr_b32 s18, s13, 7
	v_add_u32_e32 v131, s6, v162
	v_cmp_lt_i32_e32 vcc, -1, v132
	v_add_u32_e32 v180, v161, v165
	ds_read_b128 v[176:179], v180
	s_and_saveexec_b64 s[6:7], vcc
	s_cbranch_execz .LBB0_2442
	v_add_u32_e32 v133, v161, v163
	ds_read_b128 v[172:175], v133
	v_lshrrev_b32_e32 v132, 8, v132
	v_mul_u32_u24_e32 v132, s12, v132
	v_add_lshl_u32 v132, v132, s18, 15
	v_add3_u32 v132, v131, v167, v132
	s_waitcnt lgkmcnt(0)
	global_store_dwordx4 v132, v[172:175], s[4:5]
.LBB0_2442:
	s_or_b64 exec, exec, s[6:7]
	v_add_u32_e32 v132, s2, v164
	v_cmp_lt_i32_e32 vcc, -1, v132
	s_and_saveexec_b64 s[6:7], vcc
	s_cbranch_execz .LBB0_2313
	v_add_u32_e32 v133, v161, v165
	v_lshrrev_b32_e32 v132, 8, v132
	v_mul_u32_u24_e32 v132, s12, v132
	v_add_lshl_u32 v132, v132, s18, 15
	v_add3_u32 v131, v131, v168, v132
	s_waitcnt lgkmcnt(0)
	global_store_dwordx4 v131, v[176:179], s[4:5]
	s_branch .LBB0_2313
